# prologue silu-table loads batched; MoE block->expert table prefix reads batched (one LDS wait instead of sixteen)
# baseline (speedup 1.0000x reference)
.LBB0_1778:
	v_mov_b32_e32 v131, s84
	ds_read2_b32 v[100:101], v131 offset1:1
	v_mov_b32_e32 v131, s69
	ds_read2_b32 v[102:103], v131 offset1:1
	v_mov_b32_e32 v131, s68
	ds_read2_b32 v[104:105], v131 offset1:1
	v_mov_b32_e32 v131, s49
	ds_read2_b32 v[106:107], v131 offset1:1
	v_mov_b32_e32 v131, s8
	ds_read2_b32 v[108:109], v131 offset1:1
	v_mov_b32_e32 v131, s9
	ds_read2_b32 v[110:111], v131 offset1:1
	v_mov_b32_e32 v131, s10
	ds_read2_b32 v[112:113], v131 offset1:1
	v_mov_b32_e32 v131, s11
	ds_read2_b32 v[114:115], v131 offset1:1
	s_waitcnt lgkmcnt(6)
	v_mov_b32_e32 v131, s12
	ds_read2_b32 v[116:117], v131 offset1:1
	v_mov_b32_e32 v131, s13
	ds_read2_b32 v[118:119], v131 offset1:1
	v_mov_b32_e32 v131, s14
	ds_read2_b32 v[120:121], v131 offset1:1
	v_mov_b32_e32 v131, s15
	ds_read2_b32 v[122:123], v131 offset1:1
	v_mov_b32_e32 v131, s16
	ds_read2_b32 v[124:125], v131 offset1:1
	v_mov_b32_e32 v131, s17
	ds_read2_b32 v[126:127], v131 offset1:1
	v_mov_b32_e32 v131, s18
	ds_read2_b32 v[128:129], v131 offset1:1
	v_mov_b32_e32 v131, s19
	ds_read_b32 v130, v131
	s_waitcnt lgkmcnt(0)
	v_mov_b32_e32 v16, v100
	v_mov_b32_e32 v17, v101
	v_cmp_le_i32_e32 vcc, v16, v14
	s_nop 1
	v_cndmask_b32_e64 v15, 0, 1, vcc
	v_cmp_le_i32_e32 vcc, v17, v14
	s_nop 1
	v_cndmask_b32_e64 v16, 0, 1, vcc
	v_add_u16_e32 v15, v16, v15
	v_mov_b32_e32 v16, v102
	v_mov_b32_e32 v17, v103
	v_cmp_le_i32_e32 vcc, v16, v14
	s_nop 1
	v_cndmask_b32_e64 v16, 0, 1, vcc
	v_cmp_le_i32_e32 vcc, v17, v14
	v_add_u16_e32 v15, v15, v16
	s_nop 0
	v_cndmask_b32_e64 v16, 0, 1, vcc
	v_add_u16_e32 v15, v15, v16
	v_mov_b32_e32 v16, v104
	v_mov_b32_e32 v17, v105
	v_cmp_le_i32_e32 vcc, v16, v14
	s_nop 1
	v_cndmask_b32_e64 v16, 0, 1, vcc
	v_cmp_le_i32_e32 vcc, v17, v14
	v_add_u16_e32 v15, v15, v16
	s_nop 0
	v_cndmask_b32_e64 v16, 0, 1, vcc
	v_add_u16_e32 v15, v15, v16
	v_mov_b32_e32 v16, v106
	v_mov_b32_e32 v17, v107
	v_cmp_le_i32_e32 vcc, v16, v14
	s_nop 1
	v_cndmask_b32_e64 v16, 0, 1, vcc
	v_cmp_le_i32_e32 vcc, v17, v14
	v_add_u16_e32 v15, v15, v16
	s_nop 0
	v_cndmask_b32_e64 v16, 0, 1, vcc
	v_add_u16_e32 v15, v15, v16
	v_mov_b32_e32 v16, v108
	v_mov_b32_e32 v17, v109
	v_cmp_le_i32_e32 vcc, v16, v14
	s_nop 1
	v_cndmask_b32_e64 v16, 0, 1, vcc
	v_cmp_le_i32_e32 vcc, v17, v14
	v_add_u16_e32 v15, v15, v16
	s_nop 0
	v_cndmask_b32_e64 v16, 0, 1, vcc
	v_add_u16_e32 v15, v15, v16
	v_mov_b32_e32 v16, v110
	v_mov_b32_e32 v17, v111
	v_cmp_le_i32_e32 vcc, v16, v14
	s_nop 1
	v_cndmask_b32_e64 v16, 0, 1, vcc
	v_cmp_le_i32_e32 vcc, v17, v14
	v_add_u16_e32 v15, v15, v16
	s_nop 0
	v_cndmask_b32_e64 v16, 0, 1, vcc
	v_add_u16_e32 v15, v15, v16
	v_mov_b32_e32 v16, v112
	v_mov_b32_e32 v17, v113
	v_cmp_le_i32_e32 vcc, v16, v14
	s_nop 1
	v_cndmask_b32_e64 v16, 0, 1, vcc
	v_cmp_le_i32_e32 vcc, v17, v14
	v_add_u16_e32 v15, v15, v16
	s_nop 0
	v_cndmask_b32_e64 v16, 0, 1, vcc
	v_add_u16_e32 v15, v15, v16
	v_mov_b32_e32 v16, v114
	v_mov_b32_e32 v17, v115
	v_cmp_le_i32_e32 vcc, v16, v14
	s_nop 1
	v_cndmask_b32_e64 v16, 0, 1, vcc
	v_cmp_le_i32_e32 vcc, v17, v14
	v_add_u16_e32 v15, v15, v16
	s_nop 0
	v_cndmask_b32_e64 v16, 0, 1, vcc
	v_add_u16_e32 v15, v15, v16
	v_mov_b32_e32 v16, v116
	v_mov_b32_e32 v17, v117
	v_cmp_le_i32_e32 vcc, v16, v14
	s_nop 1
	v_cndmask_b32_e64 v16, 0, 1, vcc
	v_cmp_le_i32_e32 vcc, v17, v14
	v_add_u16_e32 v15, v15, v16
	s_nop 0
	v_cndmask_b32_e64 v16, 0, 1, vcc
	v_add_u16_e32 v15, v15, v16
	v_mov_b32_e32 v16, v118
	v_mov_b32_e32 v17, v119
	v_cmp_le_i32_e32 vcc, v16, v14
	s_nop 1
	v_cndmask_b32_e64 v16, 0, 1, vcc
	v_cmp_le_i32_e32 vcc, v17, v14
	v_add_u16_e32 v15, v15, v16
	s_nop 0
	v_cndmask_b32_e64 v16, 0, 1, vcc
	v_add_u16_e32 v15, v15, v16
	v_mov_b32_e32 v16, v120
	v_mov_b32_e32 v17, v121
	v_cmp_le_i32_e32 vcc, v16, v14
	s_nop 1
	v_cndmask_b32_e64 v16, 0, 1, vcc
	v_cmp_le_i32_e32 vcc, v17, v14
	v_add_u16_e32 v15, v15, v16
	s_nop 0
	v_cndmask_b32_e64 v16, 0, 1, vcc
	v_add_u16_e32 v15, v15, v16
	v_mov_b32_e32 v16, v122
	v_mov_b32_e32 v17, v123
	v_cmp_le_i32_e32 vcc, v16, v14
	s_nop 1
	v_cndmask_b32_e64 v16, 0, 1, vcc
	v_cmp_le_i32_e32 vcc, v17, v14
	v_add_u16_e32 v15, v15, v16
	s_nop 0
	v_cndmask_b32_e64 v16, 0, 1, vcc
	v_add_u16_e32 v15, v15, v16
	v_mov_b32_e32 v16, v124
	v_mov_b32_e32 v17, v125
	v_cmp_le_i32_e32 vcc, v16, v14
	s_nop 1
	v_cndmask_b32_e64 v16, 0, 1, vcc
	v_cmp_le_i32_e32 vcc, v17, v14
	v_add_u16_e32 v15, v15, v16
	s_nop 0
	v_cndmask_b32_e64 v16, 0, 1, vcc
	v_add_u16_e32 v15, v15, v16
	v_mov_b32_e32 v16, v126
	v_mov_b32_e32 v17, v127
	v_cmp_le_i32_e32 vcc, v16, v14
	s_nop 1
	v_cndmask_b32_e64 v16, 0, 1, vcc
	v_cmp_le_i32_e32 vcc, v17, v14
	v_add_u16_e32 v15, v15, v16
	s_nop 0
	v_cndmask_b32_e64 v16, 0, 1, vcc
	v_add_u16_e32 v15, v15, v16
	v_mov_b32_e32 v16, v128
	v_mov_b32_e32 v17, v129
	v_cmp_le_i32_e32 vcc, v16, v14
	s_nop 1
	v_cndmask_b32_e64 v16, 0, 1, vcc
	v_cmp_le_i32_e32 vcc, v17, v14
	v_add_u16_e32 v15, v15, v16
	s_nop 0
	v_cndmask_b32_e64 v16, 0, 1, vcc
	v_add_u16_e32 v15, v15, v16
	v_mov_b32_e32 v16, v130
	v_cmp_le_i32_e32 vcc, v16, v14
	s_nop 1
	v_cndmask_b32_e64 v16, 0, 1, vcc
	v_add_u16_e32 v15, v15, v16
	v_add_u32_e32 v16, 0, v13
	v_add_u32_e32 v13, 0x200, v13
	v_cmp_ge_i32_e32 vcc, v13, v12
	v_add_u32_e32 v16, 0x20400, v16
	v_add_u32_e32 v14, 0x20000, v14
	s_or_b64 s[6:7], vcc, s[6:7]
	ds_write_b8 v16, v15
	s_andn2_b64 exec, exec, s[6:7]
	s_cbranch_execnz .LBB0_1778

.LBB0_1857:
	v_mov_b32_e32 v131, s84
	ds_read2_b32 v[100:101], v131 offset1:1
	v_mov_b32_e32 v131, s69
	ds_read2_b32 v[102:103], v131 offset1:1
	v_mov_b32_e32 v131, s68
	ds_read2_b32 v[104:105], v131 offset1:1
	v_mov_b32_e32 v131, s49
	ds_read2_b32 v[106:107], v131 offset1:1
	v_mov_b32_e32 v131, s8
	ds_read2_b32 v[108:109], v131 offset1:1
	v_mov_b32_e32 v131, s9
	ds_read2_b32 v[110:111], v131 offset1:1
	v_mov_b32_e32 v131, s10
	ds_read2_b32 v[112:113], v131 offset1:1
	v_mov_b32_e32 v131, s11
	ds_read2_b32 v[114:115], v131 offset1:1
	s_waitcnt lgkmcnt(6)
	v_mov_b32_e32 v131, s12
	ds_read2_b32 v[116:117], v131 offset1:1
	v_mov_b32_e32 v131, s13
	ds_read2_b32 v[118:119], v131 offset1:1
	v_mov_b32_e32 v131, s14
	ds_read2_b32 v[120:121], v131 offset1:1
	v_mov_b32_e32 v131, s15
	ds_read2_b32 v[122:123], v131 offset1:1
	v_mov_b32_e32 v131, s16
	ds_read2_b32 v[124:125], v131 offset1:1
	v_mov_b32_e32 v131, s17
	ds_read2_b32 v[126:127], v131 offset1:1
	v_mov_b32_e32 v131, s18
	ds_read2_b32 v[128:129], v131 offset1:1
	v_mov_b32_e32 v131, s19
	ds_read_b32 v130, v131
	s_waitcnt lgkmcnt(0)
	v_mov_b32_e32 v4, v100
	v_mov_b32_e32 v5, v101
	v_cmp_le_i32_e32 vcc, v4, v3
	s_nop 1
	v_cndmask_b32_e64 v4, 0, 1, vcc
	v_cmp_le_i32_e32 vcc, v5, v3
	s_nop 1
	v_cndmask_b32_e64 v5, 0, 1, vcc
	v_add_u16_e32 v6, v5, v4
	v_mov_b32_e32 v4, v102
	v_mov_b32_e32 v5, v103
	v_cmp_le_i32_e32 vcc, v4, v3
	s_nop 1
	v_cndmask_b32_e64 v4, 0, 1, vcc
	v_cmp_le_i32_e32 vcc, v5, v3
	v_add_u16_e32 v4, v6, v4
	s_nop 0
	v_cndmask_b32_e64 v5, 0, 1, vcc
	v_add_u16_e32 v6, v4, v5
	v_mov_b32_e32 v4, v104
	v_mov_b32_e32 v5, v105
	v_cmp_le_i32_e32 vcc, v4, v3
	s_nop 1
	v_cndmask_b32_e64 v4, 0, 1, vcc
	v_cmp_le_i32_e32 vcc, v5, v3
	v_add_u16_e32 v4, v6, v4
	s_nop 0
	v_cndmask_b32_e64 v5, 0, 1, vcc
	v_add_u16_e32 v6, v4, v5
	v_mov_b32_e32 v4, v106
	v_mov_b32_e32 v5, v107
	v_cmp_le_i32_e32 vcc, v4, v3
	s_nop 1
	v_cndmask_b32_e64 v4, 0, 1, vcc
	v_cmp_le_i32_e32 vcc, v5, v3
	v_add_u16_e32 v4, v6, v4
	s_nop 0
	v_cndmask_b32_e64 v5, 0, 1, vcc
	v_add_u16_e32 v6, v4, v5
	v_mov_b32_e32 v4, v108
	v_mov_b32_e32 v5, v109
	v_cmp_le_i32_e32 vcc, v4, v3
	s_nop 1
	v_cndmask_b32_e64 v4, 0, 1, vcc
	v_cmp_le_i32_e32 vcc, v5, v3
	v_add_u16_e32 v4, v6, v4
	s_nop 0
	v_cndmask_b32_e64 v5, 0, 1, vcc
	v_add_u16_e32 v6, v4, v5
	v_mov_b32_e32 v4, v110
	v_mov_b32_e32 v5, v111
	v_cmp_le_i32_e32 vcc, v4, v3
	s_nop 1
	v_cndmask_b32_e64 v4, 0, 1, vcc
	v_cmp_le_i32_e32 vcc, v5, v3
	v_add_u16_e32 v4, v6, v4
	s_nop 0
	v_cndmask_b32_e64 v5, 0, 1, vcc
	v_add_u16_e32 v6, v4, v5
	v_mov_b32_e32 v4, v112
	v_mov_b32_e32 v5, v113
	v_cmp_le_i32_e32 vcc, v4, v3
	s_nop 1
	v_cndmask_b32_e64 v4, 0, 1, vcc
	v_cmp_le_i32_e32 vcc, v5, v3
	v_add_u16_e32 v4, v6, v4
	s_nop 0
	v_cndmask_b32_e64 v5, 0, 1, vcc
	v_add_u16_e32 v6, v4, v5
	v_mov_b32_e32 v4, v114
	v_mov_b32_e32 v5, v115
	v_cmp_le_i32_e32 vcc, v4, v3
	s_nop 1
	v_cndmask_b32_e64 v4, 0, 1, vcc
	v_cmp_le_i32_e32 vcc, v5, v3
	v_add_u16_e32 v4, v6, v4
	s_nop 0
	v_cndmask_b32_e64 v5, 0, 1, vcc
	v_add_u16_e32 v6, v4, v5
	v_mov_b32_e32 v4, v116
	v_mov_b32_e32 v5, v117
	v_cmp_le_i32_e32 vcc, v4, v3
	s_nop 1
	v_cndmask_b32_e64 v4, 0, 1, vcc
	v_cmp_le_i32_e32 vcc, v5, v3
	v_add_u16_e32 v4, v6, v4
	s_nop 0
	v_cndmask_b32_e64 v5, 0, 1, vcc
	v_add_u16_e32 v6, v4, v5
	v_mov_b32_e32 v4, v118
	v_mov_b32_e32 v5, v119
	v_cmp_le_i32_e32 vcc, v4, v3
	s_nop 1
	v_cndmask_b32_e64 v4, 0, 1, vcc
	v_cmp_le_i32_e32 vcc, v5, v3
	v_add_u16_e32 v4, v6, v4
	s_nop 0
	v_cndmask_b32_e64 v5, 0, 1, vcc
	v_add_u16_e32 v6, v4, v5
	v_mov_b32_e32 v4, v120
	v_mov_b32_e32 v5, v121
	v_cmp_le_i32_e32 vcc, v4, v3
	s_nop 1
	v_cndmask_b32_e64 v4, 0, 1, vcc
	v_cmp_le_i32_e32 vcc, v5, v3
	v_add_u16_e32 v4, v6, v4
	s_nop 0
	v_cndmask_b32_e64 v5, 0, 1, vcc
	v_add_u16_e32 v6, v4, v5
	v_mov_b32_e32 v4, v122
	v_mov_b32_e32 v5, v123
	v_cmp_le_i32_e32 vcc, v4, v3
	s_nop 1
	v_cndmask_b32_e64 v4, 0, 1, vcc
	v_cmp_le_i32_e32 vcc, v5, v3
	v_add_u16_e32 v4, v6, v4
	s_nop 0
	v_cndmask_b32_e64 v5, 0, 1, vcc
	v_add_u16_e32 v6, v4, v5
	v_mov_b32_e32 v4, v124
	v_mov_b32_e32 v5, v125
	v_cmp_le_i32_e32 vcc, v4, v3
	s_nop 1
	v_cndmask_b32_e64 v4, 0, 1, vcc
	v_cmp_le_i32_e32 vcc, v5, v3
	v_add_u16_e32 v4, v6, v4
	s_nop 0
	v_cndmask_b32_e64 v5, 0, 1, vcc
	v_add_u16_e32 v6, v4, v5
	v_mov_b32_e32 v4, v126
	v_mov_b32_e32 v5, v127
	v_cmp_le_i32_e32 vcc, v4, v3
	s_nop 1
	v_cndmask_b32_e64 v4, 0, 1, vcc
	v_cmp_le_i32_e32 vcc, v5, v3
	v_add_u16_e32 v4, v6, v4
	s_nop 0
	v_cndmask_b32_e64 v5, 0, 1, vcc
	v_add_u16_e32 v6, v4, v5
	v_mov_b32_e32 v4, v128
	v_mov_b32_e32 v5, v129
	v_cmp_le_i32_e32 vcc, v4, v3
	s_nop 1
	v_cndmask_b32_e64 v4, 0, 1, vcc
	v_cmp_le_i32_e32 vcc, v5, v3
	v_add_u16_e32 v4, v6, v4
	s_nop 0
	v_cndmask_b32_e64 v5, 0, 1, vcc
	v_add_u16_e32 v4, v4, v5
	v_mov_b32_e32 v5, v130
	v_cmp_le_i32_e32 vcc, v5, v3
	s_nop 1
	v_cndmask_b32_e64 v5, 0, 1, vcc
	v_add_u16_e32 v4, v4, v5
	v_add_u32_e32 v5, 0, v0
	v_add_u32_e32 v0, 0x200, v0
	v_cmp_ge_i32_e32 vcc, v0, v2
	v_add_u32_e32 v5, 0x20400, v5
	v_add_u32_e32 v3, 0x20000, v3
	s_or_b64 s[6:7], vcc, s[6:7]
	ds_write_b8 v5, v4
	s_andn2_b64 exec, exec, s[6:7]
	s_cbranch_execnz .LBB0_1857
